# MoE gate/up GEMM: next unit's row-table loads issued at the start of the epilogue (before its stores) so the end-of-unit wait is vmcnt(8) instead of a full store drain
# speedup vs baseline: 1.0018x; 1.0018x over previous
; #define GAS __attribute__((address_space(1)))
; __device__ __forceinline__ int launder_v(int v) { asm volatile("" : "+v"(v)); return v; }
; __device__ __forceinline__ LAS float* T0(ldsp tab, int par) { return (LAS float*)(tab) + par * 256; }
; __device__ __forceinline__ LAS float* T1(ldsp tab, int par) { return (LAS float*)(tab + 2048) + par * 256; }
; __device__ __forceinline__ LAS int*   T2(ldsp tab, int par) { return (LAS int*)(tab + 4096) + par * 256; }
; __device__ __forceinline__ LAS float* T3(ldsp tab, int par) { return (LAS float*)(tab + 6144) + par * 512; }
; #define PROB_WS() unsigned char* w_ = ws; asm volatile("" : "+s"(w_))
;     __device__ __forceinline__ void prepare(const Unit& u, int par, ldsp tab) const {
;         PROB_WS(); const GAS int* rowtok = (const GAS int*)(w_ + WS_ROWTOK); const GAS float* roww = (const GAS float*)(w_ + WS_ROWW); const GAS float* rowr = (const GAS float*)(w_ + WS_ROWR);
;         const int tid = launder_v(threadIdx.x); const int e = u.e, lt = u.lt;
;         const GAS float* bias = (const GAS float*)(w_ + WS_BEGU) + ((size_t)i * NE + e) * 2 * (2 * DFE) + (size_t)(tid >> 8) * (2 * DFE) + u.pn * 256;
;         const float bv = bias[tid & 255];
;         int rt = -1; float r = 0.f, w = 0.f;
;         if (tid < 256) { const int idx = lt * 256 + tid; if (idx < mt.p[32 + e]) { const size_t o = (size_t)e * MT + idx; rt = rowtok[o]; r = rowr[o]; w = roww[o]; } }
;         T3(tab, par)[tid] = bv;
;         if (tid < 256) { T2(tab, par)[tid] = rt; T0(tab, par)[tid] = r * (1.0f / W8_SCALE); T1(tab, par)[tid] = w * H8_SCALE; } }
.LBB0_1610:
	s_mov_b32 s96, 0
	s_and_b64 vcc, exec, s[38:39]
	s_cbranch_vccnz .Lprep_early_skip
	s_add_u32 s26, s4, s63
	s_addc_u32 s27, s5, s62
	s_mul_i32 s13, s42, 0xe000
	s_mul_hi_i32 s3, s42, 0xe000
	s_add_u32 s26, s26, s13
	s_addc_u32 s27, s27, s3
	v_lshrrev_b32_e32 v204, 8, v0
	v_mul_hi_i32_i24_e32 v205, 0x7000, v204
	v_mul_i32_i24_e32 v204, 0x7000, v204
	v_lshl_add_u64 v[204:205], s[26:27], 0, v[204:205]
	s_lshl_b32 s26, s40, 8
	s_ashr_i32 s27, s26, 31
	v_lshl_add_u64 v[204:205], s[26:27], 2, v[204:205]
	v_lshlrev_b32_sdwa v206, v241, v0 dst_sel:DWORD dst_unused:UNUSED_PAD src0_sel:DWORD src1_sel:BYTE_0
	v_mov_b32_e32 v207, v3
	v_lshl_add_u64 v[204:205], v[204:205], 0, v[206:207]
	v_add_co_u32_e32 v204, vcc, 0x284000, v204
	s_nop 1
	v_addc_co_u32_e32 v205, vcc, 0, v205, vcc
	global_load_dword v200, v[204:205], off
	v_mov_b32_e32 v201, -1
	v_mov_b32_e32 v202, 0
	v_mov_b32_e32 v203, 0
	v_cmp_gt_i32_e32 vcc, 0x100, v0
	s_and_b64 exec, exec, vcc
	s_cbranch_execz .Lprep_early_done
	s_lshl_b32 s3, s42, 2
	s_add_i32 s3, s3, 0x22900
	v_mov_b32_e32 v204, s3
	ds_read_b32 v205, v204
	v_lshl_add_u32 v206, v188, 8, v0
	s_waitcnt lgkmcnt(0)
	v_cmp_lt_i32_e32 vcc, v206, v205
	s_and_b64 exec, exec, vcc
	s_cbranch_execz .Lprep_early_done
	s_mov_b32 s26, s42
	s_ashr_i32 s27, s42, 31
	s_lshl_b64 s[26:27], s[26:27], 14
	v_ashrrev_i32_e32 v207, 31, v206
	v_lshl_add_u64 v[204:205], s[26:27], 0, v[206:207]
	v_lshl_add_u64 v[204:205], v[204:205], 2, s[4:5]
	v_add_co_u32_e32 v206, vcc, 0x5f4000, v204
	s_nop 1
	v_addc_co_u32_e32 v207, vcc, 0, v205, vcc
	v_add_co_u32_e32 v208, vcc, 0x6f4000, v204
	global_load_dword v201, v[206:207], off
	s_nop 0
	v_addc_co_u32_e32 v209, vcc, 0, v205, vcc
	v_add_co_u32_e32 v204, vcc, 0x674000, v204
	global_load_dword v203, v[208:209], off
	s_nop 0
	v_addc_co_u32_e32 v205, vcc, 0, v205, vcc
	global_load_dword v202, v[204:205], off

; #define LAS __attribute__((address_space(3)))
; __device__ __forceinline__ float ex2(float x) { return __builtin_amdgcn_exp2f(x); }
; __device__ __forceinline__ float rcpf_(float x) { return __builtin_amdgcn_rcpf(x); }
; __device__ __forceinline__ LAS float* T0(ldsp tab, int par) { return (LAS float*)(tab) + par * 256; }
; __device__ __forceinline__ LAS float* T1(ldsp tab, int par) { return (LAS float*)(tab + 2048) + par * 256; }
;     __device__ __forceinline__ void epi(const Acc& acc, const Unit& u, int par, ldsp tab, int wr, int wc, int fr, int fq) const {
;         PROB_WS(); unsigned char* act = w_ + WS_ACT;
;         const size_t pos0 = (size_t)mt.p[16 + u.e] + (size_t)u.lt * 256;
;         const LAS float* bpe = T3(tab, par) + wc * 32 + 8 * fq;
;         int rtv[8]; float rsv[8], wv[8];
; #pragma unroll
;         for (int g = 0; g < 8; ++g) { const int lr = (g >> 2) * 128 + wr * 64 + (g & 3) * 16 + fr; rtv[g] = T2(tab, par)[lr]; rsv[g] = T0(tab, par)[lr]; wv[g] = T1(tab, par)[lr]; }
; #pragma unroll
;         for (int ai = 0; ai < 2; ++ai)
; #pragma unroll
;             for (int m = 0; m < 4; ++m) { const int lr = ai * 128 + wr * 64 + m * 16 + fr; const int rt = rtv[ai * 4 + m];
;                 { const float rs = rsv[ai * 4 + m], w = wv[ai * 4 + m]; const LAS float* bp = bpe + ((rt >= 0 ? rt : 0) >> 14) * 256;
;                     const f32x4 g0 = acc[ai][0][m][0] * rs + *(const LAS f32x4*)(bp), g1 = acc[ai][0][m][1] * rs + *(const LAS f32x4*)(bp + 4);
;                     const f32x4 u0 = (acc[ai][1][m][0] * rs + *(const LAS f32x4*)(bp + 128)) * w, u1 = (acc[ai][1][m][1] * rs + *(const LAS f32x4*)(bp + 132)) * w;
;                     const f32x4 t0 = g0 * (-LOG2E), t1 = g1 * (-LOG2E);
;                     f32x4 e0, e1;
; #pragma unroll
;                     for (int j = 0; j < 4; ++j) { e0[j] = ex2(t0[j]); e1[j] = ex2(t1[j]); }
;                     const f32x4 d0 = e0 + 1.0f, d1 = e1 + 1.0f; f32x4 r0, r1;
; #pragma unroll
;                     for (int j = 0; j < 4; ++j) { r0[j] = rcpf_(d0[j]); r1[j] = rcpf_(d1[j]); }
;                     f32x4 h[2]; h[0] = (g0 * u0) * r0; h[1] = (g1 * u1) * r1;
;                     u32x2 o8; o8.x = cvt4_fp8(h[0][0], h[0][1], h[0][2], h[0][3]); o8.y = cvt4_fp8(h[1][0], h[1][1], h[1][2], h[1][3]);
;                     if (rt >= 0) gst8(act + (pos0 + lr) * DFE + u.pn * 128 + wc * 32 + 8 * fq, o8); } }
.Lprep_early_skip:
	s_lshl_b32 s26, s44, 2
	s_add_i32 s26, s26, 0
	s_and_b32 s13, s2, 1
	s_add_i32 s26, s26, 0x228c0
	v_mov_b32_e32 v4, v185
	v_mov_b32_e32 v6, s26
	s_lshl_b32 s26, s13, 10
	v_mov_b32_e32 v5, v186
	s_mov_b64 s[2:3], s[4:5]
	v_add_u32_e32 v12, s71, v4
	s_add_i32 s26, s26, 0
	ds_read_b32 v6, v6
	v_lshlrev_b32_e32 v9, 2, v12
	s_add_i32 s27, s26, 0x20000
	s_add_i32 s28, s26, 0x20800
	v_add_u32_e32 v13, s27, v9
	v_add_u32_e32 v11, s28, v9
	ds_read_b32 v10, v13 offset:704
	ds_read_b32 v8, v11 offset:704
	s_lshl_b32 s13, s13, 11
	v_ashrrev_i32_e32 v167, 31, v166
	v_add_u32_e32 v9, s26, v9
	s_add_u32 s44, s2, 0x250f4000
	s_waitcnt lgkmcnt(0)
	v_ashrrev_i32_e32 v7, 31, v6
	v_lshlrev_b64 v[34:35], 8, v[166:167]
	v_lshlrev_b32_e32 v4, 3, v5
	v_add_u32_e32 v9, 0x21000, v9
	s_addc_u32 s45, s3, 0
	s_add_i32 s2, s74, s13
	ds_read2_b32 v[32:33], v9 offset1:16
	ds_read2_b32 v[30:31], v13 offset0:16 offset1:32
	ds_read2_b32 v[28:29], v11 offset0:16 offset1:32
	ds_read2_b32 v[26:27], v9 offset0:32 offset1:48
	ds_read2_b32 v[24:25], v13 offset0:48 offset1:128
	ds_read2_b32 v[22:23], v11 offset0:48 offset1:128
	ds_read2_b32 v[20:21], v9 offset0:128 offset1:144
	ds_read2_b32 v[18:19], v13 offset0:144 offset1:160
	ds_read2_b32 v[16:17], v11 offset0:144 offset1:160
	ds_read2_b32 v[14:15], v9 offset0:160 offset1:176
	v_lshl_add_u64 v[6:7], v[34:35], 0, v[6:7]
	v_lshl_add_u32 v9, v5, 5, s2
	v_ashrrev_i32_e32 v5, 31, v4
	s_waitcnt lgkmcnt(0)
	v_cmp_lt_i32_e32 vcc, -1, v32
	s_and_saveexec_b64 s[48:49], vcc
	s_cbranch_execz .LBB0_1619
	ds_read_b32 v166, v13
	v_lshrrev_b32_e32 v13, 4, v32
	v_and_b32_e32 v13, 0x7fffc00, v13
	v_add_u32_e32 v13, v9, v13
	ds_read_b128 v[176:179], v13
	ds_read_b128 v[168:171], v13 offset:16
	s_mov_b32 s2, 0xc3e00000
	s_movk_i32 s13, 0xe00
	s_waitcnt lgkmcnt(0)
	v_pk_fma_f32 v[156:157], v[156:157], v[166:167], v[176:177] op_sel_hi:[1,0,1]
	v_pk_fma_f32 v[168:169], v[160:161], v[166:167], v[168:169] op_sel_hi:[1,0,1]
	v_pk_fma_f32 v[162:163], v[162:163], v[166:167], v[170:171] op_sel_hi:[1,0,1]
	v_mul_f32_e32 v32, 0xbfb8aa3b, v168
	v_exp_f32_e32 v32, v32
	v_pk_fma_f32 v[34:35], v[158:159], v[166:167], v[178:179] op_sel_hi:[1,0,1]
	v_add_f32_e32 v32, 1.0, v32
	v_rcp_f32_e32 v170, v32
	v_mul_f32_e32 v32, 0xbfb8aa3b, v169
	v_exp_f32_e32 v32, v32
	s_nop 0
	v_add_f32_e32 v32, 1.0, v32
	v_rcp_f32_e32 v171, v32
	v_mul_f32_e32 v32, 0xbfb8aa3b, v162
	v_exp_f32_e32 v32, v32
	s_nop 0
	v_add_f32_e32 v32, 1.0, v32
	v_rcp_f32_e32 v172, v32
	v_mul_f32_e32 v32, 0xbfb8aa3b, v163
	v_exp_f32_e32 v32, v32
	s_nop 0
	v_add_f32_e32 v32, 1.0, v32
	v_rcp_f32_e32 v173, v32
	v_mul_f32_e32 v32, 0xbfb8aa3b, v156
	v_exp_f32_e32 v32, v32
	s_nop 0
	v_add_f32_e32 v32, 1.0, v32
	v_rcp_f32_e32 v158, v32
	v_mul_f32_e32 v32, 0xbfb8aa3b, v157
	v_exp_f32_e32 v32, v32
	s_nop 0
	v_add_f32_e32 v32, 1.0, v32
	v_rcp_f32_e32 v159, v32
	v_mul_f32_e32 v32, 0xbfb8aa3b, v34
	v_exp_f32_e32 v32, v32
	s_nop 0
	v_add_f32_e32 v32, 1.0, v32
	v_rcp_f32_e32 v160, v32
	v_mul_f32_e32 v32, 0xbfb8aa3b, v35
	v_exp_f32_e32 v32, v32
	s_nop 0
	v_add_f32_e32 v32, 1.0, v32
	v_rcp_f32_e32 v161, v32
	ds_read_b32 v32, v11
	ds_read_b128 v[176:179], v13 offset:528
	s_waitcnt lgkmcnt(0)
	v_pk_fma_f32 v[154:155], v[154:155], v[166:167], v[178:179] op_sel_hi:[1,0,1]
	v_pk_fma_f32 v[152:153], v[152:153], v[166:167], v[176:177] op_sel_hi:[1,0,1]
	v_pk_mul_f32 v[178:179], v[32:33], v[154:155] op_sel_hi:[0,1]
	v_pk_mul_f32 v[176:177], v[32:33], v[152:153] op_sel_hi:[0,1]
	ds_read_b128 v[152:155], v13 offset:512
	s_waitcnt lgkmcnt(0)
	v_pk_fma_f32 v[150:151], v[150:151], v[166:167], v[154:155] op_sel_hi:[1,0,1]
	v_pk_fma_f32 v[148:149], v[148:149], v[166:167], v[152:153] op_sel_hi:[1,0,1]
	v_pk_mul_f32 v[152:153], v[162:163], v[178:179]
	v_pk_mul_f32 v[154:155], v[168:169], v[176:177]
	v_pk_mul_f32 v[152:153], v[152:153], v[172:173]
	v_pk_mul_f32 v[154:155], v[154:155], v[170:171]
	v_pk_mul_f32 v[148:149], v[32:33], v[148:149] op_sel_hi:[0,1]
	v_pk_mul_f32 v[150:151], v[32:33], v[150:151] op_sel_hi:[0,1]
	v_med3_f32 v11, v152, s2, v246
	v_med3_f32 v13, v153, s2, v246
	v_med3_f32 v32, v154, s2, v246
	v_med3_f32 v152, v155, s2, v246
	v_mov_b32_e32 v153, v3
	v_cvt_pk_fp8_f32 v153, v32, v152
	v_pk_mul_f32 v[34:35], v[34:35], v[150:151]
	v_pk_mul_f32 v[148:149], v[156:157], v[148:149]
	v_pk_mul_f32 v[34:35], v[34:35], v[160:161]
	v_pk_mul_f32 v[148:149], v[148:149], v[158:159]
	v_cvt_pk_fp8_f32 v153, v11, v13 op_sel:[0,0,1]
	v_med3_f32 v11, v34, s2, v246
	v_med3_f32 v32, v148, s2, v246
	v_med3_f32 v34, v149, s2, v246
	v_mov_b32_e32 v152, v3
	v_cvt_pk_fp8_f32 v152, v32, v34
	v_med3_f32 v13, v35, s2, v246
	v_mov_b64_e32 v[148:149], s[44:45]
	v_cvt_pk_fp8_f32 v152, v11, v13 op_sel:[0,0,1]
	v_ashrrev_i32_e32 v13, 31, v12
	v_lshl_add_u64 v[34:35], v[6:7], 0, v[12:13]
	v_mad_u64_u32 v[148:149], s[2:3], v34, s13, v[148:149]
	s_lshl_b32 s2, s12, 7
	v_mad_i32_i24 v149, v35, s13, v149
	s_ashr_i32 s3, s2, 31
	v_lshl_add_u64 v[34:35], v[148:149], 0, s[2:3]
	v_lshl_add_u64 v[34:35], v[34:35], 0, s[8:9]
	v_lshl_add_u64 v[34:35], v[34:35], 0, v[4:5]
	global_store_dwordx2 v[34:35], v[152:153], off
	s_bitset1_b32 s96, 0
	s_or_b64 exec, exec, s[48:49]
	v_cmp_lt_i32_e32 vcc, -1, v33
	s_and_saveexec_b64 s[48:49], vcc
	s_cbranch_execnz .LBB0_1620

; #define LAS __attribute__((address_space(3)))
; __device__ __forceinline__ float ex2(float x) { return __builtin_amdgcn_exp2f(x); }
; __device__ __forceinline__ float rcpf_(float x) { return __builtin_amdgcn_rcpf(x); }
;     __device__ __forceinline__ void epi(const Acc& acc, const Unit& u, int par, ldsp tab, int wr, int wc, int fr, int fq) const {
;     ...
;             for (int m = 0; m < 4; ++m) { const int lr = ai * 128 + wr * 64 + m * 16 + fr; const int rt = rtv[ai * 4 + m];
;                 { const float rs = rsv[ai * 4 + m], w = wv[ai * 4 + m]; const LAS float* bp = bpe + ((rt >= 0 ? rt : 0) >> 14) * 256;
;                     const f32x4 g0 = acc[ai][0][m][0] * rs + *(const LAS f32x4*)(bp), g1 = acc[ai][0][m][1] * rs + *(const LAS f32x4*)(bp + 4);
;                     const f32x4 u0 = (acc[ai][1][m][0] * rs + *(const LAS f32x4*)(bp + 128)) * w, u1 = (acc[ai][1][m][1] * rs + *(const LAS f32x4*)(bp + 132)) * w;
;                     const f32x4 t0 = g0 * (-LOG2E), t1 = g1 * (-LOG2E);
;                     f32x4 e0, e1;
; #pragma unroll
;                     for (int j = 0; j < 4; ++j) { e0[j] = ex2(t0[j]); e1[j] = ex2(t1[j]); }
;                     const f32x4 d0 = e0 + 1.0f, d1 = e1 + 1.0f; f32x4 r0, r1;
; #pragma unroll
;                     for (int j = 0; j < 4; ++j) { r0[j] = rcpf_(d0[j]); r1[j] = rcpf_(d1[j]); }
;                     f32x4 h[2]; h[0] = (g0 * u0) * r0; h[1] = (g1 * u1) * r1;
;                     u32x2 o8; o8.x = cvt4_fp8(h[0][0], h[0][1], h[0][2], h[0][3]); o8.y = cvt4_fp8(h[1][0], h[1][1], h[1][2], h[1][3]);
;                     if (rt >= 0) gst8(act + (pos0 + lr) * DFE + u.pn * 128 + wc * 32 + 8 * fq, o8); } }
.LBB0_1613:
	v_lshrrev_b32_e32 v11, 4, v26
	v_and_b32_e32 v11, 0x7fffc00, v11
	v_add_u32_e32 v11, v9, v11
	ds_read_b128 v[32:35], v11
	ds_read_b128 v[132:135], v11 offset:16
	v_mov_b32_e32 v26, v31
	s_mov_b32 s2, 0xc3e00000
	v_add_u32_e32 v28, 32, v12
	s_waitcnt lgkmcnt(0)
	v_pk_fma_f32 v[124:125], v[124:125], v[26:27], v[32:33] op_sel_hi:[1,0,1]
	v_pk_fma_f32 v[128:129], v[128:129], v[26:27], v[132:133] op_sel_hi:[1,0,1]
	v_pk_fma_f32 v[130:131], v[130:131], v[26:27], v[134:135] op_sel_hi:[1,0,1]
	v_mul_f32_e32 v13, 0xbfb8aa3b, v128
	v_exp_f32_e32 v13, v13
	v_pk_fma_f32 v[34:35], v[126:127], v[26:27], v[34:35] op_sel_hi:[1,0,1]
	ds_read_b128 v[30:33], v11 offset:528
	s_movk_i32 s13, 0xe00
	v_add_f32_e32 v13, 1.0, v13
	v_rcp_f32_e32 v132, v13
	v_mul_f32_e32 v13, 0xbfb8aa3b, v129
	v_exp_f32_e32 v13, v13
	s_waitcnt lgkmcnt(0)
	v_pk_fma_f32 v[32:33], v[122:123], v[26:27], v[32:33] op_sel_hi:[1,0,1]
	v_pk_fma_f32 v[30:31], v[120:121], v[26:27], v[30:31] op_sel_hi:[1,0,1]
	v_mov_b32_e32 v120, v29
	v_add_f32_e32 v13, 1.0, v13
	v_rcp_f32_e32 v133, v13
	v_mul_f32_e32 v13, 0xbfb8aa3b, v130
	v_exp_f32_e32 v13, v13
	v_pk_mul_f32 v[122:123], v[120:121], v[30:31] op_sel_hi:[0,1]
	v_pk_mul_f32 v[138:139], v[120:121], v[32:33] op_sel_hi:[0,1]
	ds_read_b128 v[30:33], v11 offset:512
	v_add_f32_e32 v13, 1.0, v13
	v_rcp_f32_e32 v134, v13
	v_mul_f32_e32 v13, 0xbfb8aa3b, v131
	v_exp_f32_e32 v13, v13
	s_waitcnt lgkmcnt(0)
	v_pk_fma_f32 v[32:33], v[118:119], v[26:27], v[32:33] op_sel_hi:[1,0,1]
	v_pk_fma_f32 v[30:31], v[116:117], v[26:27], v[30:31] op_sel_hi:[1,0,1]
	v_pk_mul_f32 v[116:117], v[130:131], v[138:139]
	v_add_f32_e32 v13, 1.0, v13
	v_rcp_f32_e32 v135, v13
	v_mul_f32_e32 v13, 0xbfb8aa3b, v124
	v_exp_f32_e32 v13, v13
	v_pk_mul_f32 v[118:119], v[128:129], v[122:123]
	v_pk_mul_f32 v[30:31], v[120:121], v[30:31] op_sel_hi:[0,1]
	v_pk_mul_f32 v[118:119], v[118:119], v[132:133]
	v_add_f32_e32 v13, 1.0, v13
	v_rcp_f32_e32 v126, v13
	v_mul_f32_e32 v13, 0xbfb8aa3b, v125
	v_exp_f32_e32 v13, v13
	v_pk_mul_f32 v[116:117], v[116:117], v[134:135]
	v_med3_f32 v26, v118, s2, v246
	v_med3_f32 v29, v119, s2, v246
	v_add_f32_e32 v13, 1.0, v13
	v_rcp_f32_e32 v127, v13
	v_mul_f32_e32 v13, 0xbfb8aa3b, v34
	v_exp_f32_e32 v13, v13
	v_pk_mul_f32 v[30:31], v[124:125], v[30:31]
	v_pk_mul_f32 v[32:33], v[120:121], v[32:33] op_sel_hi:[0,1]
	v_pk_mul_f32 v[30:31], v[30:31], v[126:127]
	v_add_f32_e32 v13, 1.0, v13
	v_rcp_f32_e32 v136, v13
	v_mul_f32_e32 v13, 0xbfb8aa3b, v35
	v_exp_f32_e32 v13, v13
	v_med3_f32 v11, v116, s2, v246
	v_mov_b32_e32 v116, v3
	v_pk_mul_f32 v[32:33], v[34:35], v[32:33]
	v_add_f32_e32 v13, 1.0, v13
	v_rcp_f32_e32 v137, v13
	v_med3_f32 v13, v117, s2, v246
	v_mov_b32_e32 v117, v3
	v_cvt_pk_fp8_f32 v117, v26, v29
	v_med3_f32 v26, v30, s2, v246
	v_med3_f32 v29, v31, s2, v246
	v_cvt_pk_fp8_f32 v116, v26, v29
	v_ashrrev_i32_e32 v29, 31, v28
	v_pk_mul_f32 v[32:33], v[32:33], v[136:137]
	v_lshl_add_u64 v[28:29], v[6:7], 0, v[28:29]
	v_mov_b64_e32 v[30:31], s[44:45]
	v_cvt_pk_fp8_f32 v117, v11, v13 op_sel:[0,0,1]
	v_med3_f32 v11, v32, s2, v246
	v_med3_f32 v13, v33, s2, v246
	v_mad_u64_u32 v[30:31], s[2:3], v28, s13, v[30:31]
	s_lshl_b32 s2, s12, 7
	v_cvt_pk_fp8_f32 v116, v11, v13 op_sel:[0,0,1]
	v_mad_i32_i24 v31, v29, s13, v31
	s_ashr_i32 s3, s2, 31
	v_lshl_add_u64 v[28:29], v[30:31], 0, s[2:3]
	v_lshl_add_u64 v[28:29], v[28:29], 0, s[8:9]
	v_lshl_add_u64 v[28:29], v[28:29], 0, v[4:5]
	global_store_dwordx2 v[28:29], v[116:117], off
	s_bitset1_b32 s96, 1
	s_or_b64 exec, exec, s[48:49]
	v_cmp_lt_i32_e32 vcc, -1, v27
	s_and_saveexec_b64 s[48:49], vcc
	s_cbranch_execnz .LBB0_1622

; #define LAS __attribute__((address_space(3)))
; __device__ __forceinline__ float ex2(float x) { return __builtin_amdgcn_exp2f(x); }
; __device__ __forceinline__ float rcpf_(float x) { return __builtin_amdgcn_rcpf(x); }
;     __device__ __forceinline__ void epi(const Acc& acc, const Unit& u, int par, ldsp tab, int wr, int wc, int fr, int fq) const {
;     ...
;             for (int m = 0; m < 4; ++m) { const int lr = ai * 128 + wr * 64 + m * 16 + fr; const int rt = rtv[ai * 4 + m];
;                 { const float rs = rsv[ai * 4 + m], w = wv[ai * 4 + m]; const LAS float* bp = bpe + ((rt >= 0 ? rt : 0) >> 14) * 256;
;                     const f32x4 g0 = acc[ai][0][m][0] * rs + *(const LAS f32x4*)(bp), g1 = acc[ai][0][m][1] * rs + *(const LAS f32x4*)(bp + 4);
;                     const f32x4 u0 = (acc[ai][1][m][0] * rs + *(const LAS f32x4*)(bp + 128)) * w, u1 = (acc[ai][1][m][1] * rs + *(const LAS f32x4*)(bp + 132)) * w;
;                     const f32x4 t0 = g0 * (-LOG2E), t1 = g1 * (-LOG2E);
;                     f32x4 e0, e1;
; #pragma unroll
;                     for (int j = 0; j < 4; ++j) { e0[j] = ex2(t0[j]); e1[j] = ex2(t1[j]); }
;                     const f32x4 d0 = e0 + 1.0f, d1 = e1 + 1.0f; f32x4 r0, r1;
; #pragma unroll
;                     for (int j = 0; j < 4; ++j) { r0[j] = rcpf_(d0[j]); r1[j] = rcpf_(d1[j]); }
;                     f32x4 h[2]; h[0] = (g0 * u0) * r0; h[1] = (g1 * u1) * r1;
;                     u32x2 o8; o8.x = cvt4_fp8(h[0][0], h[0][1], h[0][2], h[0][3]); o8.y = cvt4_fp8(h[1][0], h[1][1], h[1][2], h[1][3]);
;                     if (rt >= 0) gst8(act + (pos0 + lr) * DFE + u.pn * 128 + wc * 32 + 8 * fq, o8); } }
.LBB0_1615:
	v_lshrrev_b32_e32 v11, 4, v20
	v_and_b32_e32 v11, 0x7fffc00, v11
	v_add_u32_e32 v11, v9, v11
	ds_read_b128 v[26:29], v11
	ds_read_b128 v[30:33], v11 offset:16
	v_mov_b32_e32 v20, v25
	s_mov_b32 s2, 0xc3e00000
	v_add_u32_e32 v22, 0x80, v12
	s_waitcnt lgkmcnt(0)
	v_pk_fma_f32 v[92:93], v[92:93], v[20:21], v[26:27] op_sel_hi:[1,0,1]
	v_pk_fma_f32 v[30:31], v[96:97], v[20:21], v[30:31] op_sel_hi:[1,0,1]
	v_pk_fma_f32 v[32:33], v[98:99], v[20:21], v[32:33] op_sel_hi:[1,0,1]
	v_mul_f32_e32 v13, 0xbfb8aa3b, v30
	v_exp_f32_e32 v13, v13
	v_pk_fma_f32 v[28:29], v[94:95], v[20:21], v[28:29] op_sel_hi:[1,0,1]
	ds_read_b128 v[24:27], v11 offset:528
	s_movk_i32 s13, 0xe00
	v_add_f32_e32 v13, 1.0, v13
	v_rcp_f32_e32 v34, v13
	v_mul_f32_e32 v13, 0xbfb8aa3b, v31
	v_exp_f32_e32 v13, v13
	s_waitcnt lgkmcnt(0)
	v_pk_fma_f32 v[26:27], v[90:91], v[20:21], v[26:27] op_sel_hi:[1,0,1]
	v_pk_fma_f32 v[24:25], v[88:89], v[20:21], v[24:25] op_sel_hi:[1,0,1]
	v_mov_b32_e32 v88, v23
	v_add_f32_e32 v13, 1.0, v13
	v_rcp_f32_e32 v35, v13
	v_mul_f32_e32 v13, 0xbfb8aa3b, v32
	v_exp_f32_e32 v13, v13
	v_pk_mul_f32 v[90:91], v[88:89], v[24:25] op_sel_hi:[0,1]
	v_pk_mul_f32 v[100:101], v[88:89], v[26:27] op_sel_hi:[0,1]
	ds_read_b128 v[24:27], v11 offset:512
	v_add_f32_e32 v13, 1.0, v13
	v_rcp_f32_e32 v96, v13
	v_mul_f32_e32 v13, 0xbfb8aa3b, v33
	v_exp_f32_e32 v13, v13
	s_waitcnt lgkmcnt(0)
	v_pk_fma_f32 v[24:25], v[84:85], v[20:21], v[24:25] op_sel_hi:[1,0,1]
	v_pk_mul_f32 v[30:31], v[30:31], v[90:91]
	v_pk_mul_f32 v[24:25], v[88:89], v[24:25] op_sel_hi:[0,1]
	v_add_f32_e32 v13, 1.0, v13
	v_rcp_f32_e32 v97, v13
	v_mul_f32_e32 v13, 0xbfb8aa3b, v92
	v_exp_f32_e32 v13, v13
	v_pk_mul_f32 v[30:31], v[30:31], v[34:35]
	v_pk_fma_f32 v[26:27], v[86:87], v[20:21], v[26:27] op_sel_hi:[1,0,1]
	v_med3_f32 v20, v30, s2, v246
	v_add_f32_e32 v13, 1.0, v13
	v_rcp_f32_e32 v94, v13
	v_mul_f32_e32 v13, 0xbfb8aa3b, v93
	v_exp_f32_e32 v13, v13
	v_med3_f32 v23, v31, s2, v246
	v_mov_b32_e32 v31, v3
	v_pk_mul_f32 v[24:25], v[92:93], v[24:25]
	v_add_f32_e32 v13, 1.0, v13
	v_rcp_f32_e32 v95, v13
	v_mul_f32_e32 v13, 0xbfb8aa3b, v28
	v_exp_f32_e32 v13, v13
	v_cvt_pk_fp8_f32 v31, v20, v23
	v_pk_mul_f32 v[24:25], v[24:25], v[94:95]
	v_pk_mul_f32 v[26:27], v[88:89], v[26:27] op_sel_hi:[0,1]
	v_add_f32_e32 v13, 1.0, v13
	v_rcp_f32_e32 v98, v13
	v_mul_f32_e32 v13, 0xbfb8aa3b, v29
	v_exp_f32_e32 v13, v13
	v_pk_mul_f32 v[32:33], v[32:33], v[100:101]
	v_med3_f32 v20, v24, s2, v246
	v_med3_f32 v23, v25, s2, v246
	v_add_f32_e32 v13, 1.0, v13
	v_rcp_f32_e32 v99, v13
	v_mov_b32_e32 v30, v3
	v_pk_mul_f32 v[32:33], v[32:33], v[96:97]
	v_pk_mul_f32 v[26:27], v[28:29], v[26:27]
	v_cvt_pk_fp8_f32 v30, v20, v23
	v_ashrrev_i32_e32 v23, 31, v22
	v_med3_f32 v11, v32, s2, v246
	v_med3_f32 v13, v33, s2, v246
	v_pk_mul_f32 v[26:27], v[26:27], v[98:99]
	v_lshl_add_u64 v[22:23], v[6:7], 0, v[22:23]
	v_mov_b64_e32 v[24:25], s[44:45]
	v_cvt_pk_fp8_f32 v31, v11, v13 op_sel:[0,0,1]
	v_med3_f32 v11, v26, s2, v246
	v_med3_f32 v13, v27, s2, v246
	v_mad_u64_u32 v[24:25], s[2:3], v22, s13, v[24:25]
	s_lshl_b32 s2, s12, 7
	v_cvt_pk_fp8_f32 v30, v11, v13 op_sel:[0,0,1]
	v_mad_i32_i24 v25, v23, s13, v25
	s_ashr_i32 s3, s2, 31
	v_lshl_add_u64 v[22:23], v[24:25], 0, s[2:3]
	v_lshl_add_u64 v[22:23], v[22:23], 0, s[8:9]
	v_lshl_add_u64 v[22:23], v[22:23], 0, v[4:5]
	global_store_dwordx2 v[22:23], v[30:31], off
	s_bitset1_b32 s96, 2
	s_or_b64 exec, exec, s[48:49]
	v_cmp_lt_i32_e32 vcc, -1, v21
	s_and_saveexec_b64 s[48:49], vcc
	s_cbranch_execnz .LBB0_1624

; #define LAS __attribute__((address_space(3)))
; __device__ __forceinline__ float ex2(float x) { return __builtin_amdgcn_exp2f(x); }
; __device__ __forceinline__ float rcpf_(float x) { return __builtin_amdgcn_rcpf(x); }
;     __device__ __forceinline__ void epi(const Acc& acc, const Unit& u, int par, ldsp tab, int wr, int wc, int fr, int fq) const {
;     ...
;             for (int m = 0; m < 4; ++m) { const int lr = ai * 128 + wr * 64 + m * 16 + fr; const int rt = rtv[ai * 4 + m];
;                 { const float rs = rsv[ai * 4 + m], w = wv[ai * 4 + m]; const LAS float* bp = bpe + ((rt >= 0 ? rt : 0) >> 14) * 256;
;                     const f32x4 g0 = acc[ai][0][m][0] * rs + *(const LAS f32x4*)(bp), g1 = acc[ai][0][m][1] * rs + *(const LAS f32x4*)(bp + 4);
;                     const f32x4 u0 = (acc[ai][1][m][0] * rs + *(const LAS f32x4*)(bp + 128)) * w, u1 = (acc[ai][1][m][1] * rs + *(const LAS f32x4*)(bp + 132)) * w;
;                     const f32x4 t0 = g0 * (-LOG2E), t1 = g1 * (-LOG2E);
;                     f32x4 e0, e1;
; #pragma unroll
;                     for (int j = 0; j < 4; ++j) { e0[j] = ex2(t0[j]); e1[j] = ex2(t1[j]); }
;                     const f32x4 d0 = e0 + 1.0f, d1 = e1 + 1.0f; f32x4 r0, r1;
; #pragma unroll
;                     for (int j = 0; j < 4; ++j) { r0[j] = rcpf_(d0[j]); r1[j] = rcpf_(d1[j]); }
;                     f32x4 h[2]; h[0] = (g0 * u0) * r0; h[1] = (g1 * u1) * r1;
;                     u32x2 o8; o8.x = cvt4_fp8(h[0][0], h[0][1], h[0][2], h[0][3]); o8.y = cvt4_fp8(h[1][0], h[1][1], h[1][2], h[1][3]);
;                     if (rt >= 0) gst8(act + (pos0 + lr) * DFE + u.pn * 128 + wc * 32 + 8 * fq, o8); } }
.LBB0_1617:
	v_lshrrev_b32_e32 v11, 4, v14
	v_and_b32_e32 v11, 0x7fffc00, v11
	v_add_u32_e32 v11, v9, v11
	ds_read_b128 v[20:23], v11
	ds_read_b128 v[24:27], v11 offset:16
	v_mov_b32_e32 v14, v19
	s_mov_b32 s2, 0xc3e00000
	v_add_u32_e32 v16, 0xa0, v12
	s_waitcnt lgkmcnt(0)
	v_pk_fma_f32 v[32:33], v[60:61], v[14:15], v[20:21] op_sel_hi:[1,0,1]
	v_pk_fma_f32 v[24:25], v[64:65], v[14:15], v[24:25] op_sel_hi:[1,0,1]
	v_pk_fma_f32 v[26:27], v[66:67], v[14:15], v[26:27] op_sel_hi:[1,0,1]
	v_mul_f32_e32 v13, 0xbfb8aa3b, v24
	v_exp_f32_e32 v13, v13
	v_pk_fma_f32 v[22:23], v[62:63], v[14:15], v[22:23] op_sel_hi:[1,0,1]
	ds_read_b128 v[18:21], v11 offset:528
	s_movk_i32 s13, 0xe00
	v_add_f32_e32 v13, 1.0, v13
	v_rcp_f32_e32 v28, v13
	v_mul_f32_e32 v13, 0xbfb8aa3b, v25
	v_exp_f32_e32 v13, v13
	s_waitcnt lgkmcnt(0)
	v_pk_fma_f32 v[20:21], v[58:59], v[14:15], v[20:21] op_sel_hi:[1,0,1]
	v_pk_fma_f32 v[18:19], v[56:57], v[14:15], v[18:19] op_sel_hi:[1,0,1]
	v_mov_b32_e32 v56, v17
	v_add_f32_e32 v13, 1.0, v13
	v_rcp_f32_e32 v29, v13
	v_mul_f32_e32 v13, 0xbfb8aa3b, v26
	v_exp_f32_e32 v13, v13
	v_pk_mul_f32 v[58:59], v[56:57], v[18:19] op_sel_hi:[0,1]
	v_pk_mul_f32 v[62:63], v[56:57], v[20:21] op_sel_hi:[0,1]
	ds_read_b128 v[18:21], v11 offset:512
	v_add_f32_e32 v13, 1.0, v13
	v_rcp_f32_e32 v30, v13
	v_mul_f32_e32 v13, 0xbfb8aa3b, v27
	v_exp_f32_e32 v13, v13
	s_waitcnt lgkmcnt(0)
	v_pk_fma_f32 v[18:19], v[52:53], v[14:15], v[18:19] op_sel_hi:[1,0,1]
	v_pk_mul_f32 v[24:25], v[24:25], v[58:59]
	v_pk_mul_f32 v[18:19], v[56:57], v[18:19] op_sel_hi:[0,1]
	v_add_f32_e32 v13, 1.0, v13
	v_rcp_f32_e32 v31, v13
	v_mul_f32_e32 v13, 0xbfb8aa3b, v32
	v_exp_f32_e32 v13, v13
	v_pk_mul_f32 v[24:25], v[24:25], v[28:29]
	v_pk_fma_f32 v[20:21], v[54:55], v[14:15], v[20:21] op_sel_hi:[1,0,1]
	v_med3_f32 v14, v24, s2, v246
	v_add_f32_e32 v13, 1.0, v13
	v_rcp_f32_e32 v34, v13
	v_mul_f32_e32 v13, 0xbfb8aa3b, v33
	v_exp_f32_e32 v13, v13
	v_med3_f32 v17, v25, s2, v246
	v_mov_b32_e32 v25, v3
	v_pk_mul_f32 v[18:19], v[32:33], v[18:19]
	v_add_f32_e32 v13, 1.0, v13
	v_rcp_f32_e32 v35, v13
	v_mul_f32_e32 v13, 0xbfb8aa3b, v22
	v_exp_f32_e32 v13, v13
	v_cvt_pk_fp8_f32 v25, v14, v17
	v_pk_mul_f32 v[18:19], v[18:19], v[34:35]
	v_pk_mul_f32 v[20:21], v[56:57], v[20:21] op_sel_hi:[0,1]
	v_add_f32_e32 v13, 1.0, v13
	v_rcp_f32_e32 v60, v13
	v_mul_f32_e32 v13, 0xbfb8aa3b, v23
	v_exp_f32_e32 v13, v13
	v_pk_mul_f32 v[26:27], v[26:27], v[62:63]
	v_med3_f32 v14, v18, s2, v246
	v_med3_f32 v17, v19, s2, v246
	v_add_f32_e32 v13, 1.0, v13
	v_rcp_f32_e32 v61, v13
	v_mov_b32_e32 v24, v3
	v_pk_mul_f32 v[26:27], v[26:27], v[30:31]
	v_pk_mul_f32 v[20:21], v[22:23], v[20:21]
	v_cvt_pk_fp8_f32 v24, v14, v17
	v_ashrrev_i32_e32 v17, 31, v16
	v_med3_f32 v11, v26, s2, v246
	v_med3_f32 v13, v27, s2, v246
	v_pk_mul_f32 v[20:21], v[20:21], v[60:61]
	v_lshl_add_u64 v[16:17], v[6:7], 0, v[16:17]
	v_mov_b64_e32 v[18:19], s[44:45]
	v_cvt_pk_fp8_f32 v25, v11, v13 op_sel:[0,0,1]
	v_med3_f32 v11, v20, s2, v246
	v_med3_f32 v13, v21, s2, v246
	v_mad_u64_u32 v[18:19], s[2:3], v16, s13, v[18:19]
	s_lshl_b32 s2, s12, 7
	v_cvt_pk_fp8_f32 v24, v11, v13 op_sel:[0,0,1]
	v_mad_i32_i24 v19, v17, s13, v19
	s_ashr_i32 s3, s2, 31
	v_lshl_add_u64 v[16:17], v[18:19], 0, s[2:3]
	v_lshl_add_u64 v[16:17], v[16:17], 0, s[8:9]
	v_lshl_add_u64 v[16:17], v[16:17], 0, v[4:5]
	global_store_dwordx2 v[16:17], v[24:25], off
	s_bitset1_b32 s96, 3
	s_or_b64 exec, exec, s[48:49]
	v_cmp_lt_i32_e32 vcc, -1, v15
	s_and_saveexec_b64 s[48:49], vcc
	s_cbranch_execnz .LBB0_1626

; #define LAS __attribute__((address_space(3)))
; __device__ __forceinline__ float ex2(float x) { return __builtin_amdgcn_exp2f(x); }
; __device__ __forceinline__ float rcpf_(float x) { return __builtin_amdgcn_rcpf(x); }
;     __device__ __forceinline__ void epi(const Acc& acc, const Unit& u, int par, ldsp tab, int wr, int wc, int fr, int fq) const {
;     ...
;             for (int m = 0; m < 4; ++m) { const int lr = ai * 128 + wr * 64 + m * 16 + fr; const int rt = rtv[ai * 4 + m];
;                 { const float rs = rsv[ai * 4 + m], w = wv[ai * 4 + m]; const LAS float* bp = bpe + ((rt >= 0 ? rt : 0) >> 14) * 256;
;                     const f32x4 g0 = acc[ai][0][m][0] * rs + *(const LAS f32x4*)(bp), g1 = acc[ai][0][m][1] * rs + *(const LAS f32x4*)(bp + 4);
;                     const f32x4 u0 = (acc[ai][1][m][0] * rs + *(const LAS f32x4*)(bp + 128)) * w, u1 = (acc[ai][1][m][1] * rs + *(const LAS f32x4*)(bp + 132)) * w;
;                     const f32x4 t0 = g0 * (-LOG2E), t1 = g1 * (-LOG2E);
;                     f32x4 e0, e1;
; #pragma unroll
;                     for (int j = 0; j < 4; ++j) { e0[j] = ex2(t0[j]); e1[j] = ex2(t1[j]); }
;                     const f32x4 d0 = e0 + 1.0f, d1 = e1 + 1.0f; f32x4 r0, r1;
; #pragma unroll
;                     for (int j = 0; j < 4; ++j) { r0[j] = rcpf_(d0[j]); r1[j] = rcpf_(d1[j]); }
;                     f32x4 h[2]; h[0] = (g0 * u0) * r0; h[1] = (g1 * u1) * r1;
;                     u32x2 o8; o8.x = cvt4_fp8(h[0][0], h[0][1], h[0][2], h[0][3]); o8.y = cvt4_fp8(h[1][0], h[1][1], h[1][2], h[1][3]);
;                     if (rt >= 0) gst8(act + (pos0 + lr) * DFE + u.pn * 128 + wc * 32 + 8 * fq, o8); } }
.LBB0_1620:
	v_lshrrev_b32_e32 v11, 4, v33
	v_and_b32_e32 v11, 0x7fffc00, v11
	v_add_u32_e32 v11, v9, v11
	ds_read_b128 v[148:151], v11
	ds_read_b128 v[152:155], v11 offset:16
	s_mov_b32 s2, 0xc3e00000
	v_add_u32_e32 v32, 16, v12
	v_ashrrev_i32_e32 v33, 31, v32
	s_waitcnt lgkmcnt(0)
	v_pk_fma_f32 v[148:149], v[140:141], v[30:31], v[148:149] op_sel_hi:[1,0,1]
	v_pk_fma_f32 v[144:145], v[144:145], v[30:31], v[152:153] op_sel_hi:[1,0,1]
	v_pk_fma_f32 v[34:35], v[146:147], v[30:31], v[154:155] op_sel_hi:[1,0,1]
	v_mul_f32_e32 v13, 0xbfb8aa3b, v144
	v_exp_f32_e32 v13, v13
	v_pk_fma_f32 v[150:151], v[142:143], v[30:31], v[150:151] op_sel_hi:[1,0,1]
	ds_read_b128 v[140:143], v11 offset:528
	v_lshl_add_u64 v[32:33], v[6:7], 0, v[32:33]
	v_add_f32_e32 v13, 1.0, v13
	v_rcp_f32_e32 v146, v13
	v_mul_f32_e32 v13, 0xbfb8aa3b, v145
	v_exp_f32_e32 v13, v13
	s_waitcnt lgkmcnt(0)
	v_pk_fma_f32 v[138:139], v[138:139], v[30:31], v[142:143] op_sel_hi:[1,0,1]
	v_pk_fma_f32 v[136:137], v[136:137], v[30:31], v[140:141] op_sel_hi:[1,0,1]
	v_pk_mul_f32 v[142:143], v[28:29], v[138:139] op_sel_hi:[0,1]
	v_add_f32_e32 v13, 1.0, v13
	v_rcp_f32_e32 v147, v13
	v_mul_f32_e32 v13, 0xbfb8aa3b, v34
	v_exp_f32_e32 v13, v13
	v_pk_mul_f32 v[140:141], v[28:29], v[136:137] op_sel_hi:[0,1]
	ds_read_b128 v[136:139], v11 offset:512
	s_movk_i32 s13, 0xe00
	v_add_f32_e32 v13, 1.0, v13
	v_rcp_f32_e32 v152, v13
	v_mul_f32_e32 v13, 0xbfb8aa3b, v35
	v_exp_f32_e32 v13, v13
	s_waitcnt lgkmcnt(0)
	v_pk_fma_f32 v[132:133], v[132:133], v[30:31], v[136:137] op_sel_hi:[1,0,1]
	v_pk_mul_f32 v[34:35], v[34:35], v[142:143]
	v_pk_mul_f32 v[136:137], v[144:145], v[140:141]
	v_add_f32_e32 v13, 1.0, v13
	v_rcp_f32_e32 v153, v13
	v_mul_f32_e32 v13, 0xbfb8aa3b, v148
	v_exp_f32_e32 v13, v13
	v_pk_fma_f32 v[134:135], v[134:135], v[30:31], v[138:139] op_sel_hi:[1,0,1]
	v_pk_mul_f32 v[132:133], v[28:29], v[132:133] op_sel_hi:[0,1]
	v_pk_mul_f32 v[136:137], v[136:137], v[146:147]
	v_add_f32_e32 v13, 1.0, v13
	v_rcp_f32_e32 v154, v13
	v_mul_f32_e32 v13, 0xbfb8aa3b, v149
	v_exp_f32_e32 v13, v13
	v_pk_mul_f32 v[34:35], v[34:35], v[152:153]
	v_pk_mul_f32 v[134:135], v[28:29], v[134:135] op_sel_hi:[0,1]
	v_med3_f32 v28, v136, s2, v246
	v_add_f32_e32 v13, 1.0, v13
	v_rcp_f32_e32 v155, v13
	v_mul_f32_e32 v13, 0xbfb8aa3b, v150
	v_exp_f32_e32 v13, v13
	v_med3_f32 v30, v137, s2, v246
	v_pk_mul_f32 v[132:133], v[148:149], v[132:133]
	v_med3_f32 v11, v34, s2, v246
	v_add_f32_e32 v13, 1.0, v13
	v_rcp_f32_e32 v156, v13
	v_mul_f32_e32 v13, 0xbfb8aa3b, v151
	v_exp_f32_e32 v13, v13
	v_pk_mul_f32 v[132:133], v[132:133], v[154:155]
	v_mov_b32_e32 v34, v3
	v_pk_mul_f32 v[134:135], v[150:151], v[134:135]
	v_add_f32_e32 v13, 1.0, v13
	v_rcp_f32_e32 v157, v13
	v_med3_f32 v13, v35, s2, v246
	v_mov_b32_e32 v35, v3
	v_cvt_pk_fp8_f32 v35, v28, v30
	v_med3_f32 v28, v132, s2, v246
	v_med3_f32 v30, v133, s2, v246
	v_cvt_pk_fp8_f32 v34, v28, v30
	v_pk_mul_f32 v[134:135], v[134:135], v[156:157]
	v_mov_b64_e32 v[132:133], s[44:45]
	v_cvt_pk_fp8_f32 v35, v11, v13 op_sel:[0,0,1]
	v_med3_f32 v11, v134, s2, v246
	v_med3_f32 v13, v135, s2, v246
	v_mad_u64_u32 v[132:133], s[2:3], v32, s13, v[132:133]
	s_lshl_b32 s2, s12, 7
	v_cvt_pk_fp8_f32 v34, v11, v13 op_sel:[0,0,1]
	v_mad_i32_i24 v133, v33, s13, v133
	s_ashr_i32 s3, s2, 31
	v_lshl_add_u64 v[32:33], v[132:133], 0, s[2:3]
	v_lshl_add_u64 v[32:33], v[32:33], 0, s[8:9]
	v_lshl_add_u64 v[32:33], v[32:33], 0, v[4:5]
	global_store_dwordx2 v[32:33], v[34:35], off
	s_bitset1_b32 s96, 4
	s_or_b64 exec, exec, s[48:49]
	v_cmp_lt_i32_e32 vcc, -1, v26
	s_and_saveexec_b64 s[48:49], vcc
	s_cbranch_execnz .LBB0_1613

; #define LAS __attribute__((address_space(3)))
; __device__ __forceinline__ float ex2(float x) { return __builtin_amdgcn_exp2f(x); }
; __device__ __forceinline__ float rcpf_(float x) { return __builtin_amdgcn_rcpf(x); }
;     __device__ __forceinline__ void epi(const Acc& acc, const Unit& u, int par, ldsp tab, int wr, int wc, int fr, int fq) const {
;     ...
;             for (int m = 0; m < 4; ++m) { const int lr = ai * 128 + wr * 64 + m * 16 + fr; const int rt = rtv[ai * 4 + m];
;                 { const float rs = rsv[ai * 4 + m], w = wv[ai * 4 + m]; const LAS float* bp = bpe + ((rt >= 0 ? rt : 0) >> 14) * 256;
;                     const f32x4 g0 = acc[ai][0][m][0] * rs + *(const LAS f32x4*)(bp), g1 = acc[ai][0][m][1] * rs + *(const LAS f32x4*)(bp + 4);
;                     const f32x4 u0 = (acc[ai][1][m][0] * rs + *(const LAS f32x4*)(bp + 128)) * w, u1 = (acc[ai][1][m][1] * rs + *(const LAS f32x4*)(bp + 132)) * w;
;                     const f32x4 t0 = g0 * (-LOG2E), t1 = g1 * (-LOG2E);
;                     f32x4 e0, e1;
; #pragma unroll
;                     for (int j = 0; j < 4; ++j) { e0[j] = ex2(t0[j]); e1[j] = ex2(t1[j]); }
;                     const f32x4 d0 = e0 + 1.0f, d1 = e1 + 1.0f; f32x4 r0, r1;
; #pragma unroll
;                     for (int j = 0; j < 4; ++j) { r0[j] = rcpf_(d0[j]); r1[j] = rcpf_(d1[j]); }
;                     f32x4 h[2]; h[0] = (g0 * u0) * r0; h[1] = (g1 * u1) * r1;
;                     u32x2 o8; o8.x = cvt4_fp8(h[0][0], h[0][1], h[0][2], h[0][3]); o8.y = cvt4_fp8(h[1][0], h[1][1], h[1][2], h[1][3]);
;                     if (rt >= 0) gst8(act + (pos0 + lr) * DFE + u.pn * 128 + wc * 32 + 8 * fq, o8); } }
.LBB0_1622:
	v_lshrrev_b32_e32 v11, 4, v27
	v_and_b32_e32 v11, 0x7fffc00, v11
	v_add_u32_e32 v11, v9, v11
	ds_read_b128 v[28:31], v11
	ds_read_b128 v[32:35], v11 offset:16
	s_mov_b32 s2, 0xc3e00000
	v_add_u32_e32 v26, 48, v12
	v_ashrrev_i32_e32 v27, 31, v26
	s_waitcnt lgkmcnt(0)
	v_pk_fma_f32 v[108:109], v[108:109], v[24:25], v[28:29] op_sel_hi:[1,0,1]
	v_pk_fma_f32 v[32:33], v[112:113], v[24:25], v[32:33] op_sel_hi:[1,0,1]
	v_pk_fma_f32 v[34:35], v[114:115], v[24:25], v[34:35] op_sel_hi:[1,0,1]
	v_mul_f32_e32 v13, 0xbfb8aa3b, v32
	v_exp_f32_e32 v13, v13
	v_pk_fma_f32 v[110:111], v[110:111], v[24:25], v[30:31] op_sel_hi:[1,0,1]
	ds_read_b128 v[28:31], v11 offset:528
	v_lshl_add_u64 v[26:27], v[6:7], 0, v[26:27]
	v_add_f32_e32 v13, 1.0, v13
	v_rcp_f32_e32 v112, v13
	v_mul_f32_e32 v13, 0xbfb8aa3b, v33
	v_exp_f32_e32 v13, v13
	s_waitcnt lgkmcnt(0)
	v_pk_fma_f32 v[30:31], v[106:107], v[24:25], v[30:31] op_sel_hi:[1,0,1]
	v_pk_fma_f32 v[28:29], v[104:105], v[24:25], v[28:29] op_sel_hi:[1,0,1]
	v_pk_mul_f32 v[106:107], v[22:23], v[30:31] op_sel_hi:[0,1]
	v_add_f32_e32 v13, 1.0, v13
	v_rcp_f32_e32 v113, v13
	v_mul_f32_e32 v13, 0xbfb8aa3b, v34
	v_exp_f32_e32 v13, v13
	v_pk_mul_f32 v[104:105], v[22:23], v[28:29] op_sel_hi:[0,1]
	ds_read_b128 v[28:31], v11 offset:512
	v_pk_mul_f32 v[32:33], v[32:33], v[104:105]
	v_add_f32_e32 v13, 1.0, v13
	v_rcp_f32_e32 v114, v13
	v_mul_f32_e32 v13, 0xbfb8aa3b, v35
	v_exp_f32_e32 v13, v13
	s_waitcnt lgkmcnt(0)
	v_pk_fma_f32 v[28:29], v[100:101], v[24:25], v[28:29] op_sel_hi:[1,0,1]
	v_pk_fma_f32 v[30:31], v[102:103], v[24:25], v[30:31] op_sel_hi:[1,0,1]
	v_pk_mul_f32 v[28:29], v[22:23], v[28:29] op_sel_hi:[0,1]
	v_add_f32_e32 v13, 1.0, v13
	v_rcp_f32_e32 v115, v13
	v_mul_f32_e32 v13, 0xbfb8aa3b, v108
	v_exp_f32_e32 v13, v13
	v_pk_mul_f32 v[32:33], v[32:33], v[112:113]
	v_pk_mul_f32 v[30:31], v[22:23], v[30:31] op_sel_hi:[0,1]
	v_med3_f32 v22, v32, s2, v246
	v_add_f32_e32 v13, 1.0, v13
	v_rcp_f32_e32 v116, v13
	v_mul_f32_e32 v13, 0xbfb8aa3b, v109
	v_exp_f32_e32 v13, v13
	v_med3_f32 v24, v33, s2, v246
	v_mov_b32_e32 v33, v3
	v_pk_mul_f32 v[28:29], v[108:109], v[28:29]
	v_add_f32_e32 v13, 1.0, v13
	v_rcp_f32_e32 v117, v13
	v_mul_f32_e32 v13, 0xbfb8aa3b, v110
	v_exp_f32_e32 v13, v13
	v_cvt_pk_fp8_f32 v33, v22, v24
	v_pk_mul_f32 v[28:29], v[28:29], v[116:117]
	v_pk_mul_f32 v[34:35], v[34:35], v[106:107]
	v_add_f32_e32 v13, 1.0, v13
	v_rcp_f32_e32 v118, v13
	v_mul_f32_e32 v13, 0xbfb8aa3b, v111
	v_exp_f32_e32 v13, v13
	v_med3_f32 v22, v28, s2, v246
	v_med3_f32 v24, v29, s2, v246
	v_mov_b32_e32 v32, v3
	v_add_f32_e32 v13, 1.0, v13
	v_rcp_f32_e32 v119, v13
	v_pk_mul_f32 v[34:35], v[34:35], v[114:115]
	v_pk_mul_f32 v[30:31], v[110:111], v[30:31]
	v_cvt_pk_fp8_f32 v32, v22, v24
	v_med3_f32 v11, v34, s2, v246
	v_med3_f32 v13, v35, s2, v246
	v_pk_mul_f32 v[30:31], v[30:31], v[118:119]
	v_mov_b64_e32 v[28:29], s[44:45]
	s_movk_i32 s13, 0xe00
	v_cvt_pk_fp8_f32 v33, v11, v13 op_sel:[0,0,1]
	v_med3_f32 v11, v30, s2, v246
	v_med3_f32 v13, v31, s2, v246
	v_mad_u64_u32 v[28:29], s[2:3], v26, s13, v[28:29]
	s_lshl_b32 s2, s12, 7
	v_cvt_pk_fp8_f32 v32, v11, v13 op_sel:[0,0,1]
	v_mad_i32_i24 v29, v27, s13, v29
	s_ashr_i32 s3, s2, 31
	v_lshl_add_u64 v[26:27], v[28:29], 0, s[2:3]
	v_lshl_add_u64 v[26:27], v[26:27], 0, s[8:9]
	v_lshl_add_u64 v[26:27], v[26:27], 0, v[4:5]
	global_store_dwordx2 v[26:27], v[32:33], off
	s_bitset1_b32 s96, 5
	s_or_b64 exec, exec, s[48:49]
	v_cmp_lt_i32_e32 vcc, -1, v20
	s_and_saveexec_b64 s[48:49], vcc
	s_cbranch_execnz .LBB0_1615

; #define LAS __attribute__((address_space(3)))
; __device__ __forceinline__ float ex2(float x) { return __builtin_amdgcn_exp2f(x); }
; __device__ __forceinline__ float rcpf_(float x) { return __builtin_amdgcn_rcpf(x); }
;     __device__ __forceinline__ void epi(const Acc& acc, const Unit& u, int par, ldsp tab, int wr, int wc, int fr, int fq) const {
;     ...
;             for (int m = 0; m < 4; ++m) { const int lr = ai * 128 + wr * 64 + m * 16 + fr; const int rt = rtv[ai * 4 + m];
;                 { const float rs = rsv[ai * 4 + m], w = wv[ai * 4 + m]; const LAS float* bp = bpe + ((rt >= 0 ? rt : 0) >> 14) * 256;
;                     const f32x4 g0 = acc[ai][0][m][0] * rs + *(const LAS f32x4*)(bp), g1 = acc[ai][0][m][1] * rs + *(const LAS f32x4*)(bp + 4);
;                     const f32x4 u0 = (acc[ai][1][m][0] * rs + *(const LAS f32x4*)(bp + 128)) * w, u1 = (acc[ai][1][m][1] * rs + *(const LAS f32x4*)(bp + 132)) * w;
;                     const f32x4 t0 = g0 * (-LOG2E), t1 = g1 * (-LOG2E);
;                     f32x4 e0, e1;
; #pragma unroll
;                     for (int j = 0; j < 4; ++j) { e0[j] = ex2(t0[j]); e1[j] = ex2(t1[j]); }
;                     const f32x4 d0 = e0 + 1.0f, d1 = e1 + 1.0f; f32x4 r0, r1;
; #pragma unroll
;                     for (int j = 0; j < 4; ++j) { r0[j] = rcpf_(d0[j]); r1[j] = rcpf_(d1[j]); }
;                     f32x4 h[2]; h[0] = (g0 * u0) * r0; h[1] = (g1 * u1) * r1;
;                     u32x2 o8; o8.x = cvt4_fp8(h[0][0], h[0][1], h[0][2], h[0][3]); o8.y = cvt4_fp8(h[1][0], h[1][1], h[1][2], h[1][3]);
;                     if (rt >= 0) gst8(act + (pos0 + lr) * DFE + u.pn * 128 + wc * 32 + 8 * fq, o8); } }
.LBB0_1624:
	v_lshrrev_b32_e32 v11, 4, v21
	v_and_b32_e32 v11, 0x7fffc00, v11
	v_add_u32_e32 v11, v9, v11
	ds_read_b128 v[22:25], v11
	ds_read_b128 v[26:29], v11 offset:16
	s_mov_b32 s2, 0xc3e00000
	v_add_u32_e32 v20, 0x90, v12
	v_ashrrev_i32_e32 v21, 31, v20
	s_waitcnt lgkmcnt(0)
	v_pk_fma_f32 v[76:77], v[76:77], v[18:19], v[22:23] op_sel_hi:[1,0,1]
	v_pk_fma_f32 v[26:27], v[80:81], v[18:19], v[26:27] op_sel_hi:[1,0,1]
	v_pk_fma_f32 v[28:29], v[82:83], v[18:19], v[28:29] op_sel_hi:[1,0,1]
	v_mul_f32_e32 v13, 0xbfb8aa3b, v26
	v_exp_f32_e32 v13, v13
	v_pk_fma_f32 v[34:35], v[78:79], v[18:19], v[24:25] op_sel_hi:[1,0,1]
	ds_read_b128 v[22:25], v11 offset:528
	v_lshl_add_u64 v[20:21], v[6:7], 0, v[20:21]
	v_add_f32_e32 v13, 1.0, v13
	v_rcp_f32_e32 v30, v13
	v_mul_f32_e32 v13, 0xbfb8aa3b, v27
	v_exp_f32_e32 v13, v13
	s_waitcnt lgkmcnt(0)
	v_pk_fma_f32 v[24:25], v[74:75], v[18:19], v[24:25] op_sel_hi:[1,0,1]
	v_pk_fma_f32 v[22:23], v[72:73], v[18:19], v[22:23] op_sel_hi:[1,0,1]
	v_pk_mul_f32 v[74:75], v[16:17], v[24:25] op_sel_hi:[0,1]
	v_add_f32_e32 v13, 1.0, v13
	v_rcp_f32_e32 v31, v13
	v_mul_f32_e32 v13, 0xbfb8aa3b, v28
	v_exp_f32_e32 v13, v13
	v_pk_mul_f32 v[72:73], v[16:17], v[22:23] op_sel_hi:[0,1]
	ds_read_b128 v[22:25], v11 offset:512
	v_pk_mul_f32 v[26:27], v[26:27], v[72:73]
	v_add_f32_e32 v13, 1.0, v13
	v_rcp_f32_e32 v32, v13
	v_mul_f32_e32 v13, 0xbfb8aa3b, v29
	v_exp_f32_e32 v13, v13
	s_waitcnt lgkmcnt(0)
	v_pk_fma_f32 v[22:23], v[68:69], v[18:19], v[22:23] op_sel_hi:[1,0,1]
	v_pk_fma_f32 v[24:25], v[70:71], v[18:19], v[24:25] op_sel_hi:[1,0,1]
	v_pk_mul_f32 v[22:23], v[16:17], v[22:23] op_sel_hi:[0,1]
	v_add_f32_e32 v13, 1.0, v13
	v_rcp_f32_e32 v33, v13
	v_mul_f32_e32 v13, 0xbfb8aa3b, v76
	v_exp_f32_e32 v13, v13
	v_pk_mul_f32 v[26:27], v[26:27], v[30:31]
	v_pk_mul_f32 v[24:25], v[16:17], v[24:25] op_sel_hi:[0,1]
	v_med3_f32 v16, v26, s2, v246
	v_add_f32_e32 v13, 1.0, v13
	v_rcp_f32_e32 v78, v13
	v_mul_f32_e32 v13, 0xbfb8aa3b, v77
	v_exp_f32_e32 v13, v13
	v_med3_f32 v18, v27, s2, v246
	v_mov_b32_e32 v27, v3
	v_pk_mul_f32 v[22:23], v[76:77], v[22:23]
	v_add_f32_e32 v13, 1.0, v13
	v_rcp_f32_e32 v79, v13
	v_mul_f32_e32 v13, 0xbfb8aa3b, v34
	v_exp_f32_e32 v13, v13
	v_cvt_pk_fp8_f32 v27, v16, v18
	v_pk_mul_f32 v[22:23], v[22:23], v[78:79]
	v_pk_mul_f32 v[28:29], v[28:29], v[74:75]
	v_add_f32_e32 v13, 1.0, v13
	v_rcp_f32_e32 v80, v13
	v_mul_f32_e32 v13, 0xbfb8aa3b, v35
	v_exp_f32_e32 v13, v13
	v_med3_f32 v16, v22, s2, v246
	v_med3_f32 v18, v23, s2, v246
	v_mov_b32_e32 v26, v3
	v_add_f32_e32 v13, 1.0, v13
	v_rcp_f32_e32 v81, v13
	v_pk_mul_f32 v[28:29], v[28:29], v[32:33]
	v_pk_mul_f32 v[24:25], v[34:35], v[24:25]
	v_cvt_pk_fp8_f32 v26, v16, v18
	v_med3_f32 v11, v28, s2, v246
	v_med3_f32 v13, v29, s2, v246
	v_pk_mul_f32 v[24:25], v[24:25], v[80:81]
	v_mov_b64_e32 v[22:23], s[44:45]
	s_movk_i32 s13, 0xe00
	v_cvt_pk_fp8_f32 v27, v11, v13 op_sel:[0,0,1]
	v_med3_f32 v11, v24, s2, v246
	v_med3_f32 v13, v25, s2, v246
	v_mad_u64_u32 v[22:23], s[2:3], v20, s13, v[22:23]
	s_lshl_b32 s2, s12, 7
	v_cvt_pk_fp8_f32 v26, v11, v13 op_sel:[0,0,1]
	v_mad_i32_i24 v23, v21, s13, v23
	s_ashr_i32 s3, s2, 31
	v_lshl_add_u64 v[20:21], v[22:23], 0, s[2:3]
	v_lshl_add_u64 v[20:21], v[20:21], 0, s[8:9]
	v_lshl_add_u64 v[20:21], v[20:21], 0, v[4:5]
	global_store_dwordx2 v[20:21], v[26:27], off
	s_bitset1_b32 s96, 6
	s_or_b64 exec, exec, s[48:49]
	v_cmp_lt_i32_e32 vcc, -1, v14
	s_and_saveexec_b64 s[48:49], vcc
	s_cbranch_execnz .LBB0_1617

; template <class P, bool ALIGN_EPI>
; __device__ __forceinline__ void gemm_phase(ldsp lds, ldsp tab, const P& S) {
;     ...
;         if (has_next && S.dry < 2) S.prepare(nxt, (ui + 1) & 1, tab);
;     __device__ __forceinline__ void epi(const Acc& acc, const Unit& u, int par, ldsp tab, int wr, int wc, int fr, int fq) const {
;     ...
;                     f32x4 h[2]; h[0] = (g0 * u0) * r0; h[1] = (g1 * u1) * r1;
;                     u32x2 o8; o8.x = cvt4_fp8(h[0][0], h[0][1], h[0][2], h[0][3]); o8.y = cvt4_fp8(h[1][0], h[1][1], h[1][2], h[1][3]);
;                     if (rt >= 0) gst8(act + (pos0 + lr) * DFE + u.pn * 128 + wc * 32 + 8 * fq, o8); } }
.LBB0_1626:
	v_lshrrev_b32_e32 v11, 4, v15
	v_and_b32_e32 v11, 0x7fffc00, v11
	v_add_u32_e32 v9, v9, v11
	ds_read_b128 v[14:17], v9 offset:528
	ds_read_b128 v[20:23], v9
	ds_read_b128 v[24:27], v9 offset:16
	s_mov_b32 s2, 0xc3e00000
	v_add_u32_e32 v12, 0xb0, v12
	s_movk_i32 s13, 0xe00
	s_waitcnt lgkmcnt(0)
	v_pk_fma_f32 v[16:17], v[50:51], v[10:11], v[16:17] op_sel_hi:[1,0,1]
	v_pk_fma_f32 v[28:29], v[44:45], v[10:11], v[24:25] op_sel_hi:[1,0,1]
	v_pk_fma_f32 v[14:15], v[48:49], v[10:11], v[14:15] op_sel_hi:[1,0,1]
	v_pk_fma_f32 v[26:27], v[46:47], v[10:11], v[26:27] op_sel_hi:[1,0,1]
	v_mul_f32_e32 v11, 0xbfb8aa3b, v28
	v_exp_f32_e32 v11, v11
	v_pk_mul_f32 v[14:15], v[8:9], v[14:15] op_sel_hi:[0,1]
	v_pk_mul_f32 v[16:17], v[8:9], v[16:17] op_sel_hi:[0,1]
	v_pk_mul_f32 v[16:17], v[16:17], v[26:27]
	v_add_f32_e32 v11, 1.0, v11
	v_rcp_f32_e32 v30, v11
	v_mul_f32_e32 v11, 0xbfb8aa3b, v29
	v_exp_f32_e32 v11, v11
	v_pk_mul_f32 v[14:15], v[14:15], v[28:29]
	v_add_f32_e32 v11, 1.0, v11
	v_rcp_f32_e32 v31, v11
	v_mul_f32_e32 v11, 0xbfb8aa3b, v26
	v_exp_f32_e32 v11, v11
	v_pk_mul_f32 v[14:15], v[14:15], v[30:31]
	s_nop 0
	v_med3_f32 v14, v14, s2, v246
	v_add_f32_e32 v11, 1.0, v11
	v_rcp_f32_e32 v32, v11
	v_mul_f32_e32 v11, 0xbfb8aa3b, v27
	v_exp_f32_e32 v11, v11
	s_nop 0
	v_add_f32_e32 v11, 1.0, v11
	v_pk_fma_f32 v[20:21], v[40:41], v[10:11], v[20:21] op_sel_hi:[1,0,1]
	v_rcp_f32_e32 v33, v11
	v_pk_fma_f32 v[18:19], v[42:43], v[10:11], v[22:23] op_sel_hi:[1,0,1]
	v_mul_f32_e32 v11, 0xbfb8aa3b, v20
	v_exp_f32_e32 v11, v11
	ds_read_b128 v[40:43], v9 offset:512
	v_pk_mul_f32 v[16:17], v[16:17], v[32:33]
	v_add_f32_e32 v11, 1.0, v11
	v_rcp_f32_e32 v22, v11
	v_mul_f32_e32 v11, 0xbfb8aa3b, v21
	v_exp_f32_e32 v11, v11
	v_med3_f32 v13, v16, s2, v246
	v_med3_f32 v16, v17, s2, v246
	v_med3_f32 v17, v15, s2, v246
	v_add_f32_e32 v11, 1.0, v11
	v_rcp_f32_e32 v23, v11
	v_mul_f32_e32 v11, 0xbfb8aa3b, v18
	v_exp_f32_e32 v11, v11
	v_mov_b32_e32 v15, v3
	v_cvt_pk_fp8_f32 v15, v14, v17
	v_mov_b32_e32 v14, v3
	v_add_f32_e32 v11, 1.0, v11
	v_rcp_f32_e32 v24, v11
	v_mul_f32_e32 v11, 0xbfb8aa3b, v19
	v_exp_f32_e32 v11, v11
	v_cvt_pk_fp8_f32 v15, v13, v16 op_sel:[0,0,1]
	v_ashrrev_i32_e32 v13, 31, v12
	v_lshl_add_u64 v[6:7], v[6:7], 0, v[12:13]
	v_add_f32_e32 v11, 1.0, v11
	v_rcp_f32_e32 v25, v11
	s_waitcnt lgkmcnt(0)
	v_pk_fma_f32 v[34:35], v[38:39], v[10:11], v[42:43] op_sel_hi:[1,0,1]
	v_pk_fma_f32 v[10:11], v[36:37], v[10:11], v[40:41] op_sel_hi:[1,0,1]
	s_nop 0
	v_pk_mul_f32 v[10:11], v[8:9], v[10:11] op_sel_hi:[0,1]
	v_pk_mul_f32 v[10:11], v[20:21], v[10:11]
	v_pk_mul_f32 v[8:9], v[8:9], v[34:35] op_sel_hi:[0,1]
	v_pk_mul_f32 v[10:11], v[10:11], v[22:23]
	v_pk_mul_f32 v[8:9], v[18:19], v[8:9]
	v_med3_f32 v10, v10, s2, v246
	v_med3_f32 v11, v11, s2, v246
	v_cvt_pk_fp8_f32 v14, v10, v11
	v_pk_mul_f32 v[8:9], v[8:9], v[24:25]
	s_nop 0
	v_med3_f32 v8, v8, s2, v246
	v_med3_f32 v9, v9, s2, v246
	v_cvt_pk_fp8_f32 v14, v8, v9 op_sel:[0,0,1]
	v_mov_b64_e32 v[8:9], s[44:45]
	v_mad_u64_u32 v[8:9], s[2:3], v6, s13, v[8:9]
	s_lshl_b32 s2, s12, 7
	v_mad_i32_i24 v9, v7, s13, v9
	s_ashr_i32 s3, s2, 31
	v_lshl_add_u64 v[6:7], v[8:9], 0, s[2:3]
	v_lshl_add_u64 v[6:7], v[6:7], 0, s[8:9]
	v_lshl_add_u64 v[4:5], v[6:7], 0, v[4:5]
	global_store_dwordx2 v[4:5], v[14:15], off
	s_bitset1_b32 s96, 7
	s_or_b64 exec, exec, s[48:49]
	s_and_b64 vcc, exec, s[38:39]
	s_mov_b64 s[12:13], -1
	s_cbranch_vccnz .LBB0_1587
.LBB0_1627:
	s_cmp_eq_u32 s96, 0xff
	s_cbranch_scc0 .Lprep_late_w0
	s_waitcnt vmcnt(8)
	s_branch .Lprep_late_go

; #define GAS __attribute__((address_space(1)))
; __device__ __forceinline__ int launder_v(int v) { asm volatile("" : "+v"(v)); return v; }
; __device__ __forceinline__ LAS float* T0(ldsp tab, int par) { return (LAS float*)(tab) + par * 256; }
; __device__ __forceinline__ LAS float* T1(ldsp tab, int par) { return (LAS float*)(tab + 2048) + par * 256; }
; __device__ __forceinline__ LAS int*   T2(ldsp tab, int par) { return (LAS int*)(tab + 4096) + par * 256; }
; __device__ __forceinline__ LAS float* T3(ldsp tab, int par) { return (LAS float*)(tab + 6144) + par * 512; }
; #define PROB_WS() unsigned char* w_ = ws; asm volatile("" : "+s"(w_))
;     __device__ __forceinline__ void prepare(const Unit& u, int par, ldsp tab) const {
;         PROB_WS(); const GAS int* rowtok = (const GAS int*)(w_ + WS_ROWTOK); const GAS float* roww = (const GAS float*)(w_ + WS_ROWW); const GAS float* rowr = (const GAS float*)(w_ + WS_ROWR);
;         const int tid = launder_v(threadIdx.x); const int e = u.e, lt = u.lt;
;         const GAS float* bias = (const GAS float*)(w_ + WS_BEGU) + ((size_t)i * NE + e) * 2 * (2 * DFE) + (size_t)(tid >> 8) * (2 * DFE) + u.pn * 256;
;         const float bv = bias[tid & 255];
;         int rt = -1; float r = 0.f, w = 0.f;
;         if (tid < 256) { const int idx = lt * 256 + tid; if (idx < mt.p[32 + e]) { const size_t o = (size_t)e * MT + idx; rt = rowtok[o]; r = rowr[o]; w = roww[o]; } }
;         T3(tab, par)[tid] = bv;
;         if (tid < 256) { T2(tab, par)[tid] = rt; T0(tab, par)[tid] = r * (1.0f / W8_SCALE); T1(tab, par)[tid] = w * H8_SCALE; } }
.Lprep_late_go:
	s_and_b32 s2, s79, 1
	v_lshlrev_b32_e32 v6, 2, v0
	s_lshl_b32 s3, s2, 11
	s_lshl_b32 s2, s2, 10
	v_add_u32_e32 v8, s3, v6
	v_add_u32_e32 v8, 0x21800, v8
	ds_write_b32 v8, v200
	v_cmp_gt_i32_e32 vcc, 0x100, v0
	s_and_b64 exec, exec, vcc
	s_cbranch_execz .Lprep_late_done
	s_mov_b32 s26, 0x41800000
	s_mov_b32 s27, 0x3c800000
	v_pk_mul_f32 v[4:5], v[202:203], s[26:27]
	v_add_u32_e32 v6, s2, v6
	v_add_u32_e32 v8, 0x20800, v6
	v_add_u32_e32 v9, 0x20000, v6
	v_add_u32_e32 v6, 0x21000, v6
	ds_write_b32 v6, v201
	ds_write_b32 v9, v5
	ds_write_b32 v8, v4
.Lprep_late_done:
	s_mov_b64 exec, -1
	s_andn2_b64 vcc, exec, s[16:17]
	s_cbranch_vccnz .LBB0_1586
